# P7: x16 output scale folded into the MFMA E8M0 block scale (exact), 64 v_pk_mul_f32 per unit removed from the epilogue (store-data WAR pads kept)
# baseline (speedup 1.0000x reference)
; #define PG8_STAGE(bufoff, gbase, voff) do { _Pragma("unroll") for (int _i = 0; _i < 2; ++_i) { unsigned keep_; \
;         asm volatile("s_mov_b32 %0, m0\n\ts_mov_b32 m0, %3\n\ts_nop 0\n\tglobal_load_lds_dwordx4 %1, %2\n\ts_mov_b32 m0, %0" : "=&s"(keep_) : "v"((voff)[_i]), "s"((const char*)(gbase)), "s"(ldsb + (unsigned)((bufoff) + _i * 8192)) : "memory"); } } while (0)
; #define PG8_WAIT_V(n) asm volatile("s_waitcnt vmcnt(" #n ")" ::: "memory")
; #define PG8_BAR __builtin_amdgcn_s_barrier()
; #define LAS __attribute__((address_space(3)))
; template <class Epi, class Sched, bool ALIGN_EPI, bool FP8 = false>
; __device__ __forceinline__ void gemm_phase(PG8_LAS unsigned char* lds, const Gemm g, const Sched& S, const Epi& E, const int wid, const int lane) {
;     ...
;     const char* cA = GA ? (const char*)g.A : (const char*)g.A + (size_t)cur.pm * tstep; const char* cB = (const char*)g.Bt + (size_t)cur.pn * tstep;
;     PG8_STAGE(PG8_SB(0, 0), cB, voffB); PG8_STAGE(PG8_SB(0, 1), cB + hstep, voffB); PG8_STAGE(PG8_SA(0, 0), cA, vc0); PG8_STAGE(PG8_SA(0, 1), cA + hstepA, vc1);
;     if (wr == 1) PG8_BAR;
;     PG8_WAIT_V(2); PG8_BAR;
;     PG8_STAGE(PG8_SB(1, 0), cB + kstep, voffB); PG8_STAGE(PG8_SA(1, 0), cA + kstep, vc0); PG8_STAGE(PG8_SB(1, 1), cB + hstep + kstep, voffB);
;     PG8_WAIT_V(6); PG8_BAR;
; template <int l>
; __device__ __forceinline__ void layer_phases(Frame& F, const XcdBarrier& bar, const int lo, const int hi) {
;     ...
;             MoeOrder<false, 8> S{F.G, (int)blockIdx.x, tb[65] * 8, (const LAS int*)(F.lds + TILEE_OFF), tb, (const LAS int*)(F.lds + CNT_OFF), (const int*)(ws + WS_LIST), (unsigned)EH};
;             const bf16* WL = (const bf16*)(ws + WS_W + (size_t)l * W_LAYER);
;             pg8::Gemm g{(const void*)(ws + WS_ACT), (const void*)(WL + W_2_OFF / 2), EH, 127 - WSHIFT, 127 - ASHIFT};
;             EpiDown E{(unsigned char*)(ws + WS_YBUF), (const LAS int*)(F.lds + TILEE_OFF), tb, (const LAS int*)(F.lds + CNT_OFF), (const int*)(ws + WS_LIST2)};
;             pg8::gemm_phase<EpiDown, MoeOrder<false, 8>, true, true>(F.lds + RING_OFF, g, S, E, F.wave, F.lane);
.LBB0_836:
	s_lshr_b32 s5, s5, 25
	s_add_i32 s5, s4, s5
	s_bfe_u32 s26, s90, 0x20006
	v_and_b32_e32 v1, 15, v2
	s_ashr_i32 s52, s5, 7
	v_and_b32_e32 v0, 0xfffffc00, v0
	v_lshl_or_b32 v161, s18, 6, v1
	v_lshl_add_u32 v4, s18, 13, v0
	s_add_u32 s18, s56, 0x4dc00000
	s_addc_u32 s19, s57, 0
	s_add_u32 s20, s56, 0x6f600000
	s_addc_u32 s21, s57, 0
	s_add_u32 s24, s6, 0x80
	s_waitcnt vmcnt(2)
	s_barrier
	s_addc_u32 s25, s7, 0
	s_add_i32 s53, s40, 0x18000
	s_mov_b32 m0, s53
	s_nop 0
	global_load_lds_dwordx4 v162, s[24:25]
	s_add_i32 s54, s40, 0x1a000
	s_mov_b32 m0, s54
	s_nop 0
	global_load_lds_dwordx4 v166, s[24:25]
	s_add_u32 s24, s8, 0x80
	s_addc_u32 s25, s9, 0
	s_add_i32 s55, s40, 0x8000
	s_add_i32 s64, s40, 0xa000
	s_mov_b32 m0, s55
	s_nop 0
	global_load_lds_dwordx4 v160, s[24:25]
	s_add_u32 s22, s22, 0x80
	s_mov_b32 m0, s64
	s_nop 0
	global_load_lds_dwordx4 v164, s[24:25]
	s_addc_u32 s23, s23, 0
	s_add_i32 s65, s40, 0x1c000
	s_add_i32 s66, s40, 0x1e000
	v_and_b32_e32 v3, 48, v2
	s_mov_b32 m0, s65
	s_nop 0
	global_load_lds_dwordx4 v162, s[22:23]
	s_cmpk_gt_i32 s4, 0x7f
	v_lshl_or_b32 v1, v1, 6, v3
	v_lshlrev_b32_e32 v3, 2, v2
	s_mov_b32 m0, s66
	s_nop 0
	global_load_lds_dwordx4 v166, s[22:23]
	s_cselect_b64 s[22:23], -1, 0
	s_add_i32 s67, s52, -2
	s_add_i32 s68, s40, 0xc000
	v_and_b32_e32 v3, 32, v3
	v_lshl_add_u32 v0, s26, 12, v0
	s_cmpk_lt_u32 s90, 0x100
	v_bitop3_b32 v4, v1, v4, v3 bitop3:0xde
	v_bitop3_b32 v0, v1, v0, v3 bitop3:0xde
	s_waitcnt vmcnt(6)
	s_cselect_b64 s[24:25], -1, 0
	v_and_b32_e32 v1, -16, v2
	s_ashr_i32 s4, s76, 3
	v_lshl_add_u32 v163, s26, 6, v1
	s_mul_i32 s70, s4, s3
	v_cndmask_b32_e64 v1, 0, 1, s[0:1]
	v_add_u32_e32 v0, 0, v0
	s_add_i32 s69, s40, 0xe000
	s_add_i32 s70, s70, s27
	v_cmp_ne_u32_e64 s[0:1], 1, v1
	v_add_u32_e32 v165, 0x10000, v0
	v_add_u32_e32 v167, 0x14000, v0
	v_add_u32_e32 v169, 0, v4
	v_mov_b32_e32 v170, 0x7d
	v_mov_b32_e32 v171, 0x7b
	v_add_u32_e32 v172, 0x18000, v0
	v_add_u32_e32 v173, 0x1c000, v0
	s_mov_b32 s26, 0x41800000
	s_barrier
	s_branch .LBB0_839

; __device__ __forceinline__ unsigned pk4_fp8(float a, float b, float c, float d) { int r = __builtin_amdgcn_cvt_pk_fp8_f32(a, b, 0, false); r = __builtin_amdgcn_cvt_pk_fp8_f32(c, d, r, true); return (unsigned)r; }
;     __device__ __forceinline__ void operator()(const f32x4 (&acc)[2][2][4][2], const Unit& u, int wr, int wc, int fr, int fq) const {
;         const int col0 = (u.pn & 7) * 256 + wc * 64 + 16 * fq;
;         const int e = tileE[u.pm], lbase = (u.pm - tb[e]) * 256 + wr * 64 + fr, ce = cnt[e];
;         const float ysc = (float)(1 << YSHIFT);
;         int drow[2][4];
; #pragma unroll
;         for (int ai = 0; ai < 2; ++ai)
; #pragma unroll
;             for (int m = 0; m < 4; ++m) { const int local = lbase + ai * HALF + m * 16; drow[ai][m] = (e >= NE) ? (local * 7 + 6) : ((local < ce) ? list2[(size_t)e * LISTCAP + local] : 7 * T); }
; #pragma unroll
;         for (int ai = 0; ai < 2; ++ai)
; #pragma unroll
;             for (int m = 0; m < 4; ++m) { unsigned char* rowp = O + (size_t)drow[ai][m] * D + col0;
;                 const f32x4 a0 = acc[ai][0][m][0] * ysc, a1 = acc[ai][0][m][1] * ysc, b0 = acc[ai][1][m][0] * ysc, b1 = acc[ai][1][m][1] * ysc;
;                 v4u w; w.x = pk4_fp8(a0[0], a0[1], a0[2], a0[3]); w.y = pk4_fp8(a1[0], a1[1], a1[2], a1[3]); w.z = pk4_fp8(b0[0], b0[1], b0[2], b0[3]); w.w = pk4_fp8(b1[0], b1[1], b1[2], b1[3]);
;                 *(v4u*)rowp = w; }
;     }
.LBB0_903:
	v_mov_b32_e32 v18, 0
	v_cvt_pk_fp8_f32 v18, v156, v157
	v_mov_b32_e32 v19, 0
	v_mov_b32_e32 v20, 0
	v_mov_b32_e32 v21, 0
	v_cvt_pk_fp8_f32 v19, v152, v153
	v_cvt_pk_fp8_f32 v20, v148, v149
	v_cvt_pk_fp8_f32 v21, v144, v145
	s_lshl_b32 s6, s73, 8
	s_and_b32 s6, s6, 0x700
	s_waitcnt vmcnt(0)
	v_ashrrev_i32_e32 v11, 31, v10
	v_cvt_pk_fp8_f32 v18, v158, v159 op_sel:[0,0,1]
	v_cvt_pk_fp8_f32 v19, v154, v155 op_sel:[0,0,1]
	v_cvt_pk_fp8_f32 v20, v150, v151 op_sel:[0,0,1]
	v_cvt_pk_fp8_f32 v21, v146, v147 op_sel:[0,0,1]
	v_add_u32_e32 v16, s6, v163
	v_lshlrev_b64 v[10:11], 11, v[10:11]
	v_ashrrev_i32_e32 v17, 31, v16
	v_lshl_add_u64 v[10:11], s[18:19], 0, v[10:11]
	v_lshl_add_u64 v[10:11], v[10:11], 0, v[16:17]
	global_store_dwordx4 v[10:11], v[18:21], off
	s_nop 1
	v_mov_b32_e32 v18, 0
	v_cvt_pk_fp8_f32 v18, v140, v141
	v_mov_b32_e32 v19, 0
	v_mov_b32_e32 v20, 0
	v_mov_b32_e32 v21, 0
	v_cvt_pk_fp8_f32 v19, v136, v137
	v_cvt_pk_fp8_f32 v20, v132, v133
	v_cvt_pk_fp8_f32 v21, v128, v129
	v_ashrrev_i32_e32 v15, 31, v14
	v_cvt_pk_fp8_f32 v18, v142, v143 op_sel:[0,0,1]
	v_cvt_pk_fp8_f32 v19, v138, v139 op_sel:[0,0,1]
	v_cvt_pk_fp8_f32 v20, v134, v135 op_sel:[0,0,1]
	v_cvt_pk_fp8_f32 v21, v130, v131 op_sel:[0,0,1]
	v_lshlrev_b64 v[10:11], 11, v[14:15]
	v_lshl_add_u64 v[10:11], s[18:19], 0, v[10:11]
	v_lshl_add_u64 v[10:11], v[10:11], 0, v[16:17]
	global_store_dwordx4 v[10:11], v[18:21], off
	s_nop 1
	v_mov_b32_e32 v19, 0
	v_mov_b32_e32 v18, 0
	v_cvt_pk_fp8_f32 v19, v120, v121
	v_mov_b32_e32 v20, 0
	v_mov_b32_e32 v21, 0
	v_cvt_pk_fp8_f32 v18, v124, v125
	v_cvt_pk_fp8_f32 v20, v116, v117
	v_cvt_pk_fp8_f32 v21, v112, v113
	v_ashrrev_i32_e32 v13, 31, v12
	v_cvt_pk_fp8_f32 v18, v126, v127 op_sel:[0,0,1]
	v_cvt_pk_fp8_f32 v19, v122, v123 op_sel:[0,0,1]
	v_cvt_pk_fp8_f32 v20, v118, v119 op_sel:[0,0,1]
	v_cvt_pk_fp8_f32 v21, v114, v115 op_sel:[0,0,1]
	v_lshlrev_b64 v[10:11], 11, v[12:13]
	v_lshl_add_u64 v[10:11], s[18:19], 0, v[10:11]
	v_lshl_add_u64 v[10:11], v[10:11], 0, v[16:17]
	global_store_dwordx4 v[10:11], v[18:21], off
	s_nop 1
	v_mov_b32_e32 v10, 0
	v_cvt_pk_fp8_f32 v10, v108, v109
	v_mov_b32_e32 v11, 0
	v_mov_b32_e32 v12, 0
	v_mov_b32_e32 v13, 0
	v_cvt_pk_fp8_f32 v11, v104, v105
	v_cvt_pk_fp8_f32 v12, v100, v101
	v_cvt_pk_fp8_f32 v13, v96, v97
	v_ashrrev_i32_e32 v9, 31, v8
	v_cvt_pk_fp8_f32 v10, v110, v111 op_sel:[0,0,1]
	v_cvt_pk_fp8_f32 v11, v106, v107 op_sel:[0,0,1]
	v_cvt_pk_fp8_f32 v12, v102, v103 op_sel:[0,0,1]
	v_cvt_pk_fp8_f32 v13, v98, v99 op_sel:[0,0,1]
	v_lshlrev_b64 v[8:9], 11, v[8:9]
	v_lshl_add_u64 v[8:9], s[18:19], 0, v[8:9]
	v_lshl_add_u64 v[8:9], v[8:9], 0, v[16:17]
	global_store_dwordx4 v[8:9], v[10:13], off
	s_nop 1
	v_mov_b32_e32 v8, 0
	v_cvt_pk_fp8_f32 v8, v92, v93
	v_mov_b32_e32 v9, 0
	v_mov_b32_e32 v10, 0
	v_mov_b32_e32 v11, 0
	v_cvt_pk_fp8_f32 v9, v88, v89
	v_cvt_pk_fp8_f32 v10, v84, v85
	v_cvt_pk_fp8_f32 v11, v80, v81
	v_ashrrev_i32_e32 v7, 31, v6
	v_cvt_pk_fp8_f32 v8, v94, v95 op_sel:[0,0,1]
	v_cvt_pk_fp8_f32 v9, v90, v91 op_sel:[0,0,1]
	v_cvt_pk_fp8_f32 v10, v86, v87 op_sel:[0,0,1]
	v_cvt_pk_fp8_f32 v11, v82, v83 op_sel:[0,0,1]
	v_lshlrev_b64 v[6:7], 11, v[6:7]
	v_lshl_add_u64 v[6:7], s[18:19], 0, v[6:7]
	v_lshl_add_u64 v[6:7], v[6:7], 0, v[16:17]
	global_store_dwordx4 v[6:7], v[8:11], off
	s_nop 1
	v_mov_b32_e32 v6, 0
	v_cvt_pk_fp8_f32 v6, v76, v77
	v_mov_b32_e32 v7, 0
	v_mov_b32_e32 v8, 0
	v_mov_b32_e32 v9, 0
	v_cvt_pk_fp8_f32 v7, v72, v73
	v_cvt_pk_fp8_f32 v8, v68, v69
	v_cvt_pk_fp8_f32 v9, v64, v65
	v_ashrrev_i32_e32 v5, 31, v4
	v_cvt_pk_fp8_f32 v6, v78, v79 op_sel:[0,0,1]
	v_cvt_pk_fp8_f32 v7, v74, v75 op_sel:[0,0,1]
	v_cvt_pk_fp8_f32 v8, v70, v71 op_sel:[0,0,1]
	v_cvt_pk_fp8_f32 v9, v66, v67 op_sel:[0,0,1]
	v_lshlrev_b64 v[4:5], 11, v[4:5]
	v_lshl_add_u64 v[4:5], s[18:19], 0, v[4:5]
	v_lshl_add_u64 v[4:5], v[4:5], 0, v[16:17]
	global_store_dwordx4 v[4:5], v[6:9], off
	s_nop 1
	v_mov_b32_e32 v4, 0
	v_cvt_pk_fp8_f32 v4, v60, v61
	v_mov_b32_e32 v5, 0
	v_mov_b32_e32 v6, 0
	v_mov_b32_e32 v7, 0
	v_cvt_pk_fp8_f32 v5, v56, v57
	v_cvt_pk_fp8_f32 v6, v52, v53
	v_cvt_pk_fp8_f32 v7, v48, v49
	v_ashrrev_i32_e32 v3, 31, v2
	v_cvt_pk_fp8_f32 v4, v62, v63 op_sel:[0,0,1]
	v_cvt_pk_fp8_f32 v5, v58, v59 op_sel:[0,0,1]
	v_cvt_pk_fp8_f32 v6, v54, v55 op_sel:[0,0,1]
	v_cvt_pk_fp8_f32 v7, v50, v51 op_sel:[0,0,1]
	v_lshlrev_b64 v[2:3], 11, v[2:3]
	v_lshl_add_u64 v[2:3], s[18:19], 0, v[2:3]
	v_lshl_add_u64 v[2:3], v[2:3], 0, v[16:17]
	global_store_dwordx4 v[2:3], v[4:7], off
	s_nop 1
	v_mov_b32_e32 v2, 0
	v_cvt_pk_fp8_f32 v2, v44, v45
	v_mov_b32_e32 v3, 0
	v_mov_b32_e32 v4, 0
	v_mov_b32_e32 v5, 0
	v_cvt_pk_fp8_f32 v3, v40, v41
	v_cvt_pk_fp8_f32 v4, v36, v37
	v_cvt_pk_fp8_f32 v5, v32, v33
	s_waitcnt lgkmcnt(0)
	v_ashrrev_i32_e32 v1, 31, v0
	v_cvt_pk_fp8_f32 v2, v46, v47 op_sel:[0,0,1]
	v_cvt_pk_fp8_f32 v3, v42, v43 op_sel:[0,0,1]
	v_cvt_pk_fp8_f32 v4, v38, v39 op_sel:[0,0,1]
	v_cvt_pk_fp8_f32 v5, v34, v35 op_sel:[0,0,1]
	v_lshlrev_b64 v[0:1], 11, v[0:1]
	v_lshl_add_u64 v[0:1], s[18:19], 0, v[0:1]
	v_lshl_add_u64 v[0:1], v[0:1], 0, v[16:17]
	s_and_b64 vcc, exec, s[4:5]
	s_mov_b64 s[4:5], -1
	global_store_dwordx4 v[0:1], v[2:5], off
	s_nop 1
	s_cbranch_vccnz .LBB0_838
	s_andn2_b64 vcc, exec, s[16:17]
	s_cbranch_vccnz .LBB0_837
	s_barrier
	s_branch .LBB0_837
